# gather: ring depth 7 + intra-workgroup s_barrier at the three section boundaries of each token (wave alignment)
# speedup vs baseline: 1.0065x; 1.0065x over previous
.LBB0_1419:
	v_mov_b32_e32 v69, v1
	v_mov_b32_e32 v83, v1
	s_waitcnt vmcnt(6)
	v_dot8c_i32_i4_e32 v69, v6, v74
	v_dot8c_i32_i4_e32 v83, v6, v70
	v_dot8c_i32_i4_e32 v69, v7, v75
	v_dot8c_i32_i4_e32 v83, v7, v71
	s_add_i32 s62, s57, -15
	v_dot8c_i32_i4_e32 v69, v8, v76
	v_dot8c_i32_i4_e32 v83, v8, v72
	s_cmp_lt_u32 s56, 3
	v_dot8c_i32_i4_e32 v69, v9, v77
	v_dot8c_i32_i4_e32 v83, v9, v73
	s_cselect_b64 vcc, -1, 0
	s_nop 1
	v_lshl_add_u32 v6, v69, 4, v83
	v_cndmask_b32_e32 v83, v79, v78, vcc
	v_cvt_f32_i32_e32 v69, v6
	v_readlane_b32 s62, v83, s62
	s_lshl_b32 s62, s62, 10
	s_nop 3
	buffer_load_dwordx4 v[6:9], v0, s[92:95], s62 offen
	v_mov_b32_e32 v84, v1
	v_mov_b32_e32 v85, v1
	s_waitcnt vmcnt(6)
	v_dot8c_i32_i4_e32 v84, v14, v74
	v_dot8c_i32_i4_e32 v85, v14, v70
	v_dot8c_i32_i4_e32 v84, v15, v75
	v_dot8c_i32_i4_e32 v85, v15, v71
	v_dot8c_i32_i4_e32 v84, v16, v76
	v_dot8c_i32_i4_e32 v85, v16, v72
	s_add_i32 s62, s57, -14
	v_dot8c_i32_i4_e32 v84, v17, v77
	v_dot8c_i32_i4_e32 v85, v17, v73
	v_readlane_b32 s62, v83, s62
	s_lshl_b32 s62, s62, 10
	s_nop 0
	v_lshl_add_u32 v14, v84, 4, v85
	v_cvt_f32_i32_e32 v84, v14
	s_nop 0
	buffer_load_dwordx4 v[14:17], v0, s[92:95], s62 offen
	v_mov_b32_e32 v85, v1
	v_mov_b32_e32 v86, v1
	s_waitcnt vmcnt(6)
	v_dot8c_i32_i4_e32 v85, v30, v74
	v_dot8c_i32_i4_e32 v86, v30, v70
	v_dot8c_i32_i4_e32 v85, v31, v75
	v_dot8c_i32_i4_e32 v86, v31, v71
	v_dot8c_i32_i4_e32 v85, v32, v76
	v_dot8c_i32_i4_e32 v86, v32, v72
	s_add_i32 s62, s57, -13
	v_dot8c_i32_i4_e32 v85, v33, v77
	v_dot8c_i32_i4_e32 v86, v33, v73
	v_readlane_b32 s62, v83, s62
	s_lshl_b32 s62, s62, 10
	s_nop 0
	v_lshl_add_u32 v30, v85, 4, v86
	v_cvt_f32_i32_e32 v85, v30
	s_nop 0
	buffer_load_dwordx4 v[30:33], v0, s[92:95], s62 offen
	v_mov_b32_e32 v86, v1
	v_mov_b32_e32 v87, v1
	s_waitcnt vmcnt(6)
	v_dot8c_i32_i4_e32 v86, v46, v74
	v_dot8c_i32_i4_e32 v87, v46, v70
	v_dot8c_i32_i4_e32 v86, v47, v75
	v_dot8c_i32_i4_e32 v87, v47, v71
	v_dot8c_i32_i4_e32 v86, v48, v76
	v_dot8c_i32_i4_e32 v87, v48, v72
	s_add_i32 s62, s57, -12
	v_dot8c_i32_i4_e32 v86, v49, v77
	v_dot8c_i32_i4_e32 v87, v49, v73
	v_readlane_b32 s62, v83, s62
	s_lshl_b32 s62, s62, 10
	s_nop 0
	v_lshl_add_u32 v46, v86, 4, v87
	v_cvt_f32_i32_e32 v86, v46
	s_nop 0
	buffer_load_dwordx4 v[46:49], v0, s[92:95], s62 offen
	v_mov_b32_e32 v87, v1
	v_mov_b32_e32 v88, v1
	s_waitcnt vmcnt(6)
	v_dot8c_i32_i4_e32 v87, v2, v74
	v_dot8c_i32_i4_e32 v88, v2, v70
	v_dot8c_i32_i4_e32 v87, v3, v75
	v_dot8c_i32_i4_e32 v88, v3, v71
	v_dot8c_i32_i4_e32 v87, v4, v76
	v_dot8c_i32_i4_e32 v88, v4, v72
	s_add_i32 s62, s57, -11
	v_dot8c_i32_i4_e32 v87, v5, v77
	v_dot8c_i32_i4_e32 v88, v5, v73
	v_readlane_b32 s62, v83, s62
	s_lshl_b32 s62, s62, 10
	s_nop 0
	v_lshl_add_u32 v2, v87, 4, v88
	v_cvt_f32_i32_e32 v87, v2
	s_nop 0
	buffer_load_dwordx4 v[2:5], v0, s[92:95], s62 offen
	v_mov_b32_e32 v88, v1
	v_mov_b32_e32 v89, v1
	s_waitcnt vmcnt(6)
	v_dot8c_i32_i4_e32 v88, v22, v74
	v_dot8c_i32_i4_e32 v89, v22, v70
	v_dot8c_i32_i4_e32 v88, v23, v75
	v_dot8c_i32_i4_e32 v89, v23, v71
	v_dot8c_i32_i4_e32 v88, v24, v76
	v_dot8c_i32_i4_e32 v89, v24, v72
	s_add_i32 s62, s57, -10
	v_dot8c_i32_i4_e32 v88, v25, v77
	v_dot8c_i32_i4_e32 v89, v25, v73
	v_readlane_b32 s62, v83, s62
	s_lshl_b32 s62, s62, 10
	s_nop 0
	v_lshl_add_u32 v22, v88, 4, v89
	v_cvt_f32_i32_e32 v88, v22
	s_nop 0
	buffer_load_dwordx4 v[22:25], v0, s[92:95], s62 offen
	v_mov_b32_e32 v89, v1
	v_mov_b32_e32 v90, v1
	s_waitcnt vmcnt(6)
	v_dot8c_i32_i4_e32 v89, v38, v74
	v_dot8c_i32_i4_e32 v90, v38, v70
	v_dot8c_i32_i4_e32 v89, v39, v75
	v_dot8c_i32_i4_e32 v90, v39, v71
	v_dot8c_i32_i4_e32 v89, v40, v76
	v_dot8c_i32_i4_e32 v90, v40, v72
	s_add_i32 s62, s57, -9
	v_dot8c_i32_i4_e32 v89, v41, v77
	v_dot8c_i32_i4_e32 v90, v41, v73
	v_readlane_b32 s62, v83, s62
	s_lshl_b32 s62, s62, 10
	s_nop 0
	v_lshl_add_u32 v38, v89, 4, v90
	v_cvt_f32_i32_e32 v89, v38
	s_nop 0
	buffer_load_dwordx4 v[38:41], v0, s[92:95], s62 offen
	v_mov_b32_e32 v90, v1
	v_mov_b32_e32 v91, v1
	s_waitcnt vmcnt(6)
	v_dot8c_i32_i4_e32 v90, v54, v74
	v_dot8c_i32_i4_e32 v91, v54, v70
	v_dot8c_i32_i4_e32 v90, v55, v75
	v_dot8c_i32_i4_e32 v91, v55, v71
	v_dot8c_i32_i4_e32 v90, v56, v76
	v_dot8c_i32_i4_e32 v91, v56, v72
	s_add_i32 s62, s57, -8
	v_dot8c_i32_i4_e32 v90, v57, v77
	v_dot8c_i32_i4_e32 v91, v57, v73
	v_readlane_b32 s62, v83, s62
	s_lshl_b32 s62, s62, 10
	s_nop 0
	v_lshl_add_u32 v54, v90, 4, v91
	v_cvt_f32_i32_e32 v90, v54
	s_nop 0
	buffer_load_dwordx4 v[54:57], v0, s[92:95], s62 offen
	v_mov_b32_e32 v91, v1
	v_mov_b32_e32 v92, v1
	s_waitcnt vmcnt(6)
	v_dot8c_i32_i4_e32 v91, v10, v74
	v_dot8c_i32_i4_e32 v92, v10, v70
	v_dot8c_i32_i4_e32 v91, v11, v75
	v_dot8c_i32_i4_e32 v92, v11, v71
	v_dot8c_i32_i4_e32 v91, v12, v76
	v_dot8c_i32_i4_e32 v92, v12, v72
	s_add_i32 s62, s57, -7
	v_dot8c_i32_i4_e32 v91, v13, v77
	v_dot8c_i32_i4_e32 v92, v13, v73
	v_readlane_b32 s62, v83, s62
	s_lshl_b32 s62, s62, 10
	s_nop 0
	v_lshl_add_u32 v10, v91, 4, v92
	v_cvt_f32_i32_e32 v91, v10
	s_nop 0
	buffer_load_dwordx4 v[10:13], v0, s[92:95], s62 offen
	v_mov_b32_e32 v92, v1
	v_mov_b32_e32 v93, v1
	s_waitcnt vmcnt(6)
	v_dot8c_i32_i4_e32 v92, v26, v74
	v_dot8c_i32_i4_e32 v93, v26, v70
	v_dot8c_i32_i4_e32 v92, v27, v75
	v_dot8c_i32_i4_e32 v93, v27, v71
	v_dot8c_i32_i4_e32 v92, v28, v76
	v_dot8c_i32_i4_e32 v93, v28, v72
	s_add_i32 s62, s57, -6
	v_dot8c_i32_i4_e32 v92, v29, v77
	v_dot8c_i32_i4_e32 v93, v29, v73
	v_readlane_b32 s62, v83, s62
	s_lshl_b32 s62, s62, 10
	s_nop 0
	v_lshl_add_u32 v26, v92, 4, v93
	v_cvt_f32_i32_e32 v92, v26
	s_nop 0
	buffer_load_dwordx4 v[26:29], v0, s[92:95], s62 offen
	v_mov_b32_e32 v93, v1
	v_mov_b32_e32 v94, v1
	s_waitcnt vmcnt(6)
;     ...
;         GATHER_U_SECTION(0, g0, w0)
	v_dot8c_i32_i4_e32 v93, v42, v74
	v_dot8c_i32_i4_e32 v94, v42, v70
	v_dot8c_i32_i4_e32 v93, v43, v75
	v_dot8c_i32_i4_e32 v94, v43, v71
	v_dot8c_i32_i4_e32 v93, v44, v76
	v_dot8c_i32_i4_e32 v94, v44, v72
	s_add_i32 s62, s57, -5
	v_dot8c_i32_i4_e32 v93, v45, v77
	v_dot8c_i32_i4_e32 v94, v45, v73
	v_readlane_b32 s62, v83, s62
	s_lshl_b32 s62, s62, 10
	s_nop 0
	v_lshl_add_u32 v42, v93, 4, v94
	v_cvt_f32_i32_e32 v93, v42
	s_nop 0
	buffer_load_dwordx4 v[42:45], v0, s[92:95], s62 offen
	v_mov_b32_e32 v94, v1
	v_mov_b32_e32 v95, v1
	s_waitcnt vmcnt(6)
	v_dot8c_i32_i4_e32 v94, v58, v74
	v_dot8c_i32_i4_e32 v95, v58, v70
	v_dot8c_i32_i4_e32 v94, v59, v75
	v_dot8c_i32_i4_e32 v95, v59, v71
	v_dot8c_i32_i4_e32 v94, v60, v76
	v_dot8c_i32_i4_e32 v95, v60, v72
	s_add_i32 s62, s57, -4
	v_dot8c_i32_i4_e32 v94, v61, v77
	v_dot8c_i32_i4_e32 v95, v61, v73
	v_readlane_b32 s62, v83, s62
	s_lshl_b32 s62, s62, 10
	s_nop 0
	v_lshl_add_u32 v58, v94, 4, v95
	v_cvt_f32_i32_e32 v94, v58
	s_nop 0
	buffer_load_dwordx4 v[58:61], v0, s[92:95], s62 offen
	v_mov_b32_e32 v95, v1
	v_mov_b32_e32 v96, v1
	s_waitcnt vmcnt(6)
	v_dot8c_i32_i4_e32 v95, v18, v74
	v_dot8c_i32_i4_e32 v96, v18, v70
	v_dot8c_i32_i4_e32 v95, v19, v75
	v_dot8c_i32_i4_e32 v96, v19, v71
	v_dot8c_i32_i4_e32 v95, v20, v76
	v_dot8c_i32_i4_e32 v96, v20, v72
	s_add_i32 s62, s57, -3
	v_dot8c_i32_i4_e32 v95, v21, v77
	v_dot8c_i32_i4_e32 v96, v21, v73
	v_readlane_b32 s62, v83, s62
	s_lshl_b32 s62, s62, 10
	s_nop 0
	v_lshl_add_u32 v18, v95, 4, v96
	v_cvt_f32_i32_e32 v95, v18
	s_nop 0
	buffer_load_dwordx4 v[18:21], v0, s[92:95], s62 offen
	v_mov_b32_e32 v96, v1
	v_mov_b32_e32 v97, v1
	s_waitcnt vmcnt(6)
	v_dot8c_i32_i4_e32 v96, v34, v74
	v_dot8c_i32_i4_e32 v97, v34, v70
	v_dot8c_i32_i4_e32 v96, v35, v75
	v_dot8c_i32_i4_e32 v97, v35, v71
	v_dot8c_i32_i4_e32 v96, v36, v76
	v_dot8c_i32_i4_e32 v97, v36, v72
	s_add_i32 s62, s57, -2
	v_dot8c_i32_i4_e32 v96, v37, v77
	v_dot8c_i32_i4_e32 v97, v37, v73
	v_readlane_b32 s62, v83, s62
	s_lshl_b32 s62, s62, 10
	s_nop 0
	v_lshl_add_u32 v34, v96, 4, v97
	v_cvt_f32_i32_e32 v96, v34
	s_nop 0
	buffer_load_dwordx4 v[34:37], v0, s[92:95], s62 offen
	v_mov_b32_e32 v97, v1
	v_mov_b32_e32 v98, v1
	s_waitcnt vmcnt(6)
	v_dot8c_i32_i4_e32 v97, v50, v74
	v_dot8c_i32_i4_e32 v98, v50, v70
	v_dot8c_i32_i4_e32 v97, v51, v75
	v_dot8c_i32_i4_e32 v98, v51, v71
	v_dot8c_i32_i4_e32 v97, v52, v76
	v_dot8c_i32_i4_e32 v98, v52, v72
	s_add_i32 s62, s57, -1
	v_dot8c_i32_i4_e32 v97, v53, v77
	v_dot8c_i32_i4_e32 v98, v53, v73
	v_readlane_b32 s62, v83, s62
	s_lshl_b32 s62, s62, 10
	s_nop 0
	v_lshl_add_u32 v50, v97, 4, v98
	v_cvt_f32_i32_e32 v97, v50
	s_nop 0
	buffer_load_dwordx4 v[50:53], v0, s[92:95], s62 offen
	v_mov_b32_e32 v98, v1
	v_mov_b32_e32 v99, v1
	s_waitcnt vmcnt(6)
	v_dot8c_i32_i4_e32 v98, v62, v74
	v_dot8c_i32_i4_e32 v99, v62, v70
	v_dot8c_i32_i4_e32 v98, v63, v75
	v_dot8c_i32_i4_e32 v99, v63, v71
	v_readlane_b32 s62, v83, s57
	v_dot8c_i32_i4_e32 v98, v64, v76
	v_dot8c_i32_i4_e32 v99, v64, v72
	s_lshl_b32 s62, s62, 10
	v_dot8c_i32_i4_e32 v98, v65, v77
	v_dot8c_i32_i4_e32 v99, v65, v73
	buffer_load_dwordx4 v[62:65], v0, s[92:95], s62 offen
	s_nop 1
	v_lshl_add_u32 v83, v98, 4, v99
	v_cvt_f32_i32_e32 v83, v83
	v_cndmask_b32_e64 v98, v91, v69, s[0:1]
	v_cndmask_b32_e64 v69, v69, v91, s[0:1]
	v_cndmask_b32_e64 v91, v92, v84, s[0:1]
	v_cndmask_b32_e64 v84, v84, v92, s[0:1]
	v_cndmask_b32_e64 v92, v93, v85, s[0:1]
	v_cndmask_b32_e64 v85, v85, v93, s[0:1]
	v_cndmask_b32_e64 v93, v94, v86, s[0:1]
	v_cndmask_b32_e64 v86, v86, v94, s[0:1]
	v_cndmask_b32_e64 v94, v95, v87, s[0:1]
	v_cndmask_b32_e64 v87, v87, v95, s[0:1]
	v_cndmask_b32_e64 v95, v96, v88, s[0:1]
	v_cndmask_b32_e64 v88, v88, v96, s[0:1]
	v_cndmask_b32_e64 v96, v97, v89, s[0:1]
	v_cndmask_b32_e64 v89, v89, v97, s[0:1]
	v_cndmask_b32_e64 v97, v83, v90, s[0:1]
	v_cndmask_b32_e64 v83, v90, v83, s[0:1]
	ds_bpermute_b32 v69, v190, v69
	ds_bpermute_b32 v84, v190, v84
	ds_bpermute_b32 v85, v190, v85
	ds_bpermute_b32 v86, v190, v86
	ds_bpermute_b32 v87, v190, v87
	ds_bpermute_b32 v88, v190, v88
	ds_bpermute_b32 v89, v190, v89
	ds_bpermute_b32 v83, v190, v83
	s_waitcnt lgkmcnt(7)
	v_add_f32_e32 v69, v98, v69
	s_waitcnt lgkmcnt(6)
	v_add_f32_e32 v84, v91, v84
	s_waitcnt lgkmcnt(5)
	v_add_f32_e32 v85, v92, v85
	s_waitcnt lgkmcnt(4)
	v_add_f32_e32 v86, v93, v86
	s_waitcnt lgkmcnt(3)
	v_add_f32_e32 v87, v94, v87
	s_waitcnt lgkmcnt(2)
	v_add_f32_e32 v88, v95, v88
	s_waitcnt lgkmcnt(1)
	v_add_f32_e32 v89, v96, v89
	s_waitcnt lgkmcnt(0)
	v_add_f32_e32 v83, v97, v83
	v_cndmask_b32_e64 v90, v87, v69, s[2:3]
	v_cndmask_b32_e64 v69, v69, v87, s[2:3]
	v_cndmask_b32_e64 v87, v88, v84, s[2:3]
	v_cndmask_b32_e64 v84, v84, v88, s[2:3]
	v_cndmask_b32_e64 v88, v89, v85, s[2:3]
	v_cndmask_b32_e64 v85, v85, v89, s[2:3]
	v_cndmask_b32_e64 v89, v83, v86, s[2:3]
	v_cndmask_b32_e64 v83, v86, v83, s[2:3]
	ds_bpermute_b32 v69, v189, v69
	ds_bpermute_b32 v84, v189, v84
	ds_bpermute_b32 v85, v189, v85
	ds_bpermute_b32 v83, v189, v83
	s_add_i32 s57, s57, 16
	s_waitcnt lgkmcnt(3)
	v_add_f32_e32 v69, v90, v69
	s_waitcnt lgkmcnt(2)
	v_add_f32_e32 v84, v87, v84
	s_waitcnt lgkmcnt(1)
	v_add_f32_e32 v85, v88, v85
	s_waitcnt lgkmcnt(0)
	v_add_f32_e32 v83, v89, v83
	v_cndmask_b32_e64 v86, v85, v69, s[4:5]
	v_cndmask_b32_e64 v69, v69, v85, s[4:5]
	v_cndmask_b32_e64 v85, v83, v84, s[4:5]
	v_cndmask_b32_e64 v83, v84, v83, s[4:5]
	ds_bpermute_b32 v69, v188, v69
	ds_bpermute_b32 v83, v188, v83
	s_waitcnt lgkmcnt(1)
	v_add_f32_e32 v69, v86, v69
	s_waitcnt lgkmcnt(0)
	v_add_f32_e32 v83, v85, v83
	v_cndmask_b32_e64 v84, v83, v69, s[6:7]
	v_cndmask_b32_e64 v69, v69, v83, s[6:7]
	ds_bpermute_b32 v69, v163, v69
	s_waitcnt lgkmcnt(0)
	v_add_f32_e32 v69, v84, v69
	v_mov_b32_e32 v83, v69
	s_nop 1
	v_permlane16_swap_b32_e32 v69, v83
	v_add_f32_e32 v69, v69, v83
	v_mov_b32_e32 v83, v69
	s_nop 1
	v_permlane32_swap_b32_e32 v69, v83
	v_add_f32_e32 v69, v69, v83
	v_mul_f32_e32 v69, v66, v69
	v_fma_f32 v83, |v69|, s66, 1.0
	v_rcp_f32_e32 v83, v83
	v_mul_f32_e32 v84, v69, v69
	v_mul_f32_e32 v84, 0xbf38aa3b, v84
	v_exp_f32_e32 v84, v84
	v_fmamk_f32 v85, v83, 0x3f07dc22, v207
	v_fmaak_f32 v85, v83, v85, 0x3f35f0e3
	v_fmaak_f32 v85, v83, v85, 0xbe11a98e
	v_fmaak_f32 v85, v83, v85, 0x3e027906
	v_mul_f32_e32 v83, v83, v85
	v_mul_f32_e32 v83, v84, v83
	v_mul_f32_e32 v84, v69, v83
	v_fma_f32 v83, -v69, v83, v69
	v_cmp_gt_f32_e32 vcc, 0, v69
	s_nop 1
	v_cndmask_b32_e32 v69, v83, v84, vcc
	v_mul_f32_e32 v69, 0x3d4ccccd, v69
	v_mul_f32_e32 v69, v82, v69
	v_cmp_eq_u32_e32 vcc, s56, v193
	s_add_i32 s56, s56, 1
	s_cmpk_eq_i32 s57, 0x5f
	v_cndmask_b32_e32 v81, v81, v69, vcc
	s_cbranch_scc0 .LBB0_1419
	s_mov_b32 s56, 0
	v_mov_b32_e32 v82, 0
	s_movk_i32 s57, 0x5f
	s_barrier
.LBB0_1421:
	v_mov_b32_e32 v69, v1
	v_mov_b32_e32 v83, v1
	s_waitcnt vmcnt(6)
	v_dot8c_i32_i4_e32 v69, v6, v74
	v_dot8c_i32_i4_e32 v83, v6, v70
	v_dot8c_i32_i4_e32 v69, v7, v75
	v_dot8c_i32_i4_e32 v83, v7, v71
	v_dot8c_i32_i4_e32 v69, v8, v76
	v_dot8c_i32_i4_e32 v83, v8, v72
	s_add_i32 s62, s57, -15
	v_dot8c_i32_i4_e32 v69, v9, v77
	v_dot8c_i32_i4_e32 v83, v9, v73
	s_bitcmp0_b32 s62, 6
	s_cselect_b64 vcc, -1, 0
	s_nop 0
	v_lshl_add_u32 v6, v69, 4, v83
	v_cvt_f32_i32_e32 v69, v6
	v_cndmask_b32_e32 v6, v79, v78, vcc
	s_nop 0
	v_readlane_b32 s62, v6, s62
	s_lshl_b32 s63, s62, 10
	s_cmp_gt_u32 s56, 2
	s_cselect_b32 s62, 0x1000000, 0
	s_add_i32 s63, s63, s62
	buffer_load_dwordx4 v[6:9], v0, s[92:95], s63 offen
	v_mov_b32_e32 v83, v1
	v_mov_b32_e32 v84, v1
	s_waitcnt vmcnt(6)
	v_dot8c_i32_i4_e32 v83, v14, v74
	v_dot8c_i32_i4_e32 v84, v14, v70
	v_dot8c_i32_i4_e32 v83, v15, v75
	v_dot8c_i32_i4_e32 v84, v15, v71
	v_dot8c_i32_i4_e32 v83, v16, v76
	v_dot8c_i32_i4_e32 v84, v16, v72
	s_add_i32 s63, s57, -14
	v_dot8c_i32_i4_e32 v83, v17, v77
	v_dot8c_i32_i4_e32 v84, v17, v73
	s_bitcmp0_b32 s63, 6
	s_cselect_b64 vcc, -1, 0
	s_nop 0
	v_lshl_add_u32 v14, v83, 4, v84
	v_cvt_f32_i32_e32 v83, v14
	v_cndmask_b32_e32 v14, v79, v78, vcc
	s_nop 0
	v_readlane_b32 s63, v14, s63
	s_lshl_b32 s63, s63, 10
	s_add_i32 s63, s63, s62
	s_nop 2
	buffer_load_dwordx4 v[14:17], v0, s[92:95], s63 offen
	v_mov_b32_e32 v84, v1
	v_mov_b32_e32 v85, v1
	s_waitcnt vmcnt(6)
	v_dot8c_i32_i4_e32 v84, v30, v74
	v_dot8c_i32_i4_e32 v85, v30, v70
	v_dot8c_i32_i4_e32 v84, v31, v75
	v_dot8c_i32_i4_e32 v85, v31, v71
	v_dot8c_i32_i4_e32 v84, v32, v76
	v_dot8c_i32_i4_e32 v85, v32, v72
	s_add_i32 s63, s57, -13
	v_dot8c_i32_i4_e32 v84, v33, v77
	v_dot8c_i32_i4_e32 v85, v33, v73
	s_bitcmp0_b32 s63, 6
	s_cselect_b64 vcc, -1, 0
	s_nop 0
	v_lshl_add_u32 v30, v84, 4, v85
	v_cvt_f32_i32_e32 v84, v30
	v_cndmask_b32_e32 v30, v79, v78, vcc
	s_nop 0
	v_readlane_b32 s63, v30, s63
	s_lshl_b32 s63, s63, 10
	s_add_i32 s63, s63, s62
	s_nop 2
	buffer_load_dwordx4 v[30:33], v0, s[92:95], s63 offen
	v_mov_b32_e32 v85, v1
	v_mov_b32_e32 v86, v1
	s_waitcnt vmcnt(6)
	v_dot8c_i32_i4_e32 v85, v46, v74
	v_dot8c_i32_i4_e32 v86, v46, v70
	v_dot8c_i32_i4_e32 v85, v47, v75
	v_dot8c_i32_i4_e32 v86, v47, v71
	v_dot8c_i32_i4_e32 v85, v48, v76
	v_dot8c_i32_i4_e32 v86, v48, v72
	s_add_i32 s63, s57, -12
	v_dot8c_i32_i4_e32 v85, v49, v77
	v_dot8c_i32_i4_e32 v86, v49, v73
	s_bitcmp0_b32 s63, 6
	s_cselect_b64 vcc, -1, 0
	s_nop 0
	v_lshl_add_u32 v46, v85, 4, v86
	v_cvt_f32_i32_e32 v85, v46
	v_cndmask_b32_e32 v46, v79, v78, vcc
	s_nop 0
	v_readlane_b32 s63, v46, s63
	s_lshl_b32 s63, s63, 10
	s_add_i32 s63, s63, s62
	s_nop 2
	buffer_load_dwordx4 v[46:49], v0, s[92:95], s63 offen
	v_mov_b32_e32 v86, v1
	v_mov_b32_e32 v87, v1
	s_waitcnt vmcnt(6)
	v_dot8c_i32_i4_e32 v86, v2, v74
	v_dot8c_i32_i4_e32 v87, v2, v70
	v_dot8c_i32_i4_e32 v86, v3, v75
	v_dot8c_i32_i4_e32 v87, v3, v71
	v_dot8c_i32_i4_e32 v86, v4, v76
	v_dot8c_i32_i4_e32 v87, v4, v72
	s_add_i32 s63, s57, -11
	v_dot8c_i32_i4_e32 v86, v5, v77
	v_dot8c_i32_i4_e32 v87, v5, v73
	s_bitcmp0_b32 s63, 6
	s_cselect_b64 vcc, -1, 0
	s_nop 0
	v_lshl_add_u32 v2, v86, 4, v87
	v_cvt_f32_i32_e32 v86, v2
	v_cndmask_b32_e32 v2, v79, v78, vcc
	s_nop 0
	v_readlane_b32 s63, v2, s63
	s_lshl_b32 s63, s63, 10
	s_add_i32 s63, s63, s62
	s_nop 2
	buffer_load_dwordx4 v[2:5], v0, s[92:95], s63 offen
	v_mov_b32_e32 v87, v1
	v_mov_b32_e32 v88, v1
	s_waitcnt vmcnt(6)
	v_dot8c_i32_i4_e32 v87, v22, v74
	v_dot8c_i32_i4_e32 v88, v22, v70
	v_dot8c_i32_i4_e32 v87, v23, v75
	v_dot8c_i32_i4_e32 v88, v23, v71
	v_dot8c_i32_i4_e32 v87, v24, v76
	v_dot8c_i32_i4_e32 v88, v24, v72
	s_add_i32 s63, s57, -10
	v_dot8c_i32_i4_e32 v87, v25, v77
	v_dot8c_i32_i4_e32 v88, v25, v73
	s_bitcmp0_b32 s63, 6
	s_cselect_b64 vcc, -1, 0
	s_nop 0
	v_lshl_add_u32 v22, v87, 4, v88
	v_cvt_f32_i32_e32 v87, v22
	v_cndmask_b32_e32 v22, v79, v78, vcc
	s_nop 0
	v_readlane_b32 s63, v22, s63
	s_lshl_b32 s63, s63, 10
	s_add_i32 s63, s63, s62
	s_nop 2
	buffer_load_dwordx4 v[22:25], v0, s[92:95], s63 offen
	v_mov_b32_e32 v88, v1
	v_mov_b32_e32 v89, v1
	s_waitcnt vmcnt(6)
	v_dot8c_i32_i4_e32 v88, v38, v74
	v_dot8c_i32_i4_e32 v89, v38, v70
	v_dot8c_i32_i4_e32 v88, v39, v75
	v_dot8c_i32_i4_e32 v89, v39, v71
	v_dot8c_i32_i4_e32 v88, v40, v76
	v_dot8c_i32_i4_e32 v89, v40, v72
	s_add_i32 s63, s57, -9
	v_dot8c_i32_i4_e32 v88, v41, v77
	v_dot8c_i32_i4_e32 v89, v41, v73
	s_bitcmp0_b32 s63, 6
	s_cselect_b64 vcc, -1, 0
	s_nop 0
	v_lshl_add_u32 v38, v88, 4, v89
	v_cvt_f32_i32_e32 v88, v38
	v_cndmask_b32_e32 v38, v79, v78, vcc
	s_nop 0
	v_readlane_b32 s63, v38, s63
	s_lshl_b32 s63, s63, 10
	s_add_i32 s63, s63, s62
	s_nop 2
	buffer_load_dwordx4 v[38:41], v0, s[92:95], s63 offen
	v_mov_b32_e32 v89, v1
	v_mov_b32_e32 v90, v1
	s_waitcnt vmcnt(6)
	v_dot8c_i32_i4_e32 v89, v54, v74
	v_dot8c_i32_i4_e32 v90, v54, v70
	v_dot8c_i32_i4_e32 v89, v55, v75
	v_dot8c_i32_i4_e32 v90, v55, v71
	v_dot8c_i32_i4_e32 v89, v56, v76
	v_dot8c_i32_i4_e32 v90, v56, v72
	s_add_i32 s63, s57, -8
	v_dot8c_i32_i4_e32 v89, v57, v77
	v_dot8c_i32_i4_e32 v90, v57, v73
	s_bitcmp0_b32 s63, 6
	s_cselect_b64 vcc, -1, 0
	s_nop 0
	v_lshl_add_u32 v54, v89, 4, v90
	v_cvt_f32_i32_e32 v89, v54
	v_cndmask_b32_e32 v54, v79, v78, vcc
	s_nop 0
	v_readlane_b32 s63, v54, s63
	s_lshl_b32 s63, s63, 10
	s_add_i32 s63, s63, s62
	s_nop 2
	buffer_load_dwordx4 v[54:57], v0, s[92:95], s63 offen
	v_mov_b32_e32 v90, v1
	v_mov_b32_e32 v91, v1
	s_waitcnt vmcnt(6)
	v_dot8c_i32_i4_e32 v90, v10, v74
	v_dot8c_i32_i4_e32 v91, v10, v70
	v_dot8c_i32_i4_e32 v90, v11, v75
	v_dot8c_i32_i4_e32 v91, v11, v71
	v_dot8c_i32_i4_e32 v90, v12, v76
	v_dot8c_i32_i4_e32 v91, v12, v72
	s_add_i32 s63, s57, -7
	v_dot8c_i32_i4_e32 v90, v13, v77
	v_dot8c_i32_i4_e32 v91, v13, v73
	s_bitcmp0_b32 s63, 6
	s_cselect_b64 vcc, -1, 0
	s_nop 0
	v_lshl_add_u32 v10, v90, 4, v91
	v_cvt_f32_i32_e32 v90, v10
	v_cndmask_b32_e32 v10, v79, v78, vcc
	s_nop 0
	v_readlane_b32 s63, v10, s63
	s_lshl_b32 s63, s63, 10
	s_add_i32 s63, s63, s62
	s_nop 2
	buffer_load_dwordx4 v[10:13], v0, s[92:95], s63 offen
	v_mov_b32_e32 v91, v1
	v_mov_b32_e32 v92, v1
	s_waitcnt vmcnt(6)
	v_dot8c_i32_i4_e32 v91, v26, v74
	v_dot8c_i32_i4_e32 v92, v26, v70
	v_dot8c_i32_i4_e32 v91, v27, v75
	v_dot8c_i32_i4_e32 v92, v27, v71
	v_dot8c_i32_i4_e32 v91, v28, v76
	v_dot8c_i32_i4_e32 v92, v28, v72
	s_add_i32 s63, s57, -6
	v_dot8c_i32_i4_e32 v91, v29, v77
	v_dot8c_i32_i4_e32 v92, v29, v73
	s_bitcmp0_b32 s63, 6
	s_cselect_b64 vcc, -1, 0
	s_nop 0
	v_lshl_add_u32 v26, v91, 4, v92
	v_cvt_f32_i32_e32 v91, v26
	v_cndmask_b32_e32 v26, v79, v78, vcc
	s_nop 0
	v_readlane_b32 s63, v26, s63
	s_lshl_b32 s63, s63, 10
	s_add_i32 s63, s63, s62
	s_nop 2
	buffer_load_dwordx4 v[26:29], v0, s[92:95], s63 offen
	v_mov_b32_e32 v92, v1
	v_mov_b32_e32 v93, v1
	s_waitcnt vmcnt(6)
	v_dot8c_i32_i4_e32 v92, v42, v74
	v_dot8c_i32_i4_e32 v93, v42, v70
	v_dot8c_i32_i4_e32 v92, v43, v75
	v_dot8c_i32_i4_e32 v93, v43, v71
	v_dot8c_i32_i4_e32 v92, v44, v76
	v_dot8c_i32_i4_e32 v93, v44, v72
	s_add_i32 s63, s57, -5
	v_dot8c_i32_i4_e32 v92, v45, v77
	v_dot8c_i32_i4_e32 v93, v45, v73
	s_bitcmp0_b32 s63, 6
	s_cselect_b64 vcc, -1, 0
	s_nop 0
	v_lshl_add_u32 v42, v92, 4, v93
	v_cvt_f32_i32_e32 v92, v42
	v_cndmask_b32_e32 v42, v79, v78, vcc
	s_nop 0
	v_readlane_b32 s63, v42, s63
	s_lshl_b32 s63, s63, 10
	s_add_i32 s63, s63, s62
	s_nop 2
	buffer_load_dwordx4 v[42:45], v0, s[92:95], s63 offen
	v_mov_b32_e32 v93, v1
	v_mov_b32_e32 v94, v1
	s_waitcnt vmcnt(6)
	v_dot8c_i32_i4_e32 v93, v58, v74
	v_dot8c_i32_i4_e32 v94, v58, v70
	v_dot8c_i32_i4_e32 v93, v59, v75
	v_dot8c_i32_i4_e32 v94, v59, v71
	v_dot8c_i32_i4_e32 v93, v60, v76
	v_dot8c_i32_i4_e32 v94, v60, v72
	s_add_i32 s63, s57, -4
	v_dot8c_i32_i4_e32 v93, v61, v77
	v_dot8c_i32_i4_e32 v94, v61, v73
	s_bitcmp0_b32 s63, 6
	s_cselect_b64 vcc, -1, 0
	s_nop 0
	v_lshl_add_u32 v58, v93, 4, v94
	v_cvt_f32_i32_e32 v93, v58
	v_cndmask_b32_e32 v58, v79, v78, vcc
	s_nop 0
	v_readlane_b32 s63, v58, s63
	s_lshl_b32 s63, s63, 10
	s_add_i32 s63, s63, s62
	s_nop 2
	buffer_load_dwordx4 v[58:61], v0, s[92:95], s63 offen
	v_mov_b32_e32 v94, v1
	v_mov_b32_e32 v95, v1
	s_waitcnt vmcnt(6)
	v_dot8c_i32_i4_e32 v94, v18, v74
	v_dot8c_i32_i4_e32 v95, v18, v70
	v_dot8c_i32_i4_e32 v94, v19, v75
	v_dot8c_i32_i4_e32 v95, v19, v71
	v_dot8c_i32_i4_e32 v94, v20, v76
	v_dot8c_i32_i4_e32 v95, v20, v72
	s_add_i32 s63, s57, -3
	v_dot8c_i32_i4_e32 v94, v21, v77
	v_dot8c_i32_i4_e32 v95, v21, v73
	s_bitcmp0_b32 s63, 6
	s_cselect_b64 vcc, -1, 0
	s_nop 0
	v_lshl_add_u32 v18, v94, 4, v95
	v_cvt_f32_i32_e32 v94, v18
	v_cndmask_b32_e32 v18, v79, v78, vcc
	s_nop 0
	v_readlane_b32 s63, v18, s63
	s_lshl_b32 s63, s63, 10
	s_add_i32 s63, s63, s62
	s_nop 2
	buffer_load_dwordx4 v[18:21], v0, s[92:95], s63 offen
	v_mov_b32_e32 v95, v1
	v_mov_b32_e32 v96, v1
	s_waitcnt vmcnt(6)
	v_dot8c_i32_i4_e32 v95, v34, v74
	v_dot8c_i32_i4_e32 v96, v34, v70
	v_dot8c_i32_i4_e32 v95, v35, v75
	v_dot8c_i32_i4_e32 v96, v35, v71
	v_dot8c_i32_i4_e32 v95, v36, v76
	v_dot8c_i32_i4_e32 v96, v36, v72
	s_add_i32 s63, s57, -2
	v_dot8c_i32_i4_e32 v95, v37, v77
	v_dot8c_i32_i4_e32 v96, v37, v73
	s_bitcmp0_b32 s63, 6
	s_cselect_b64 vcc, -1, 0
	s_nop 0
	v_lshl_add_u32 v34, v95, 4, v96
	v_cvt_f32_i32_e32 v95, v34
	v_cndmask_b32_e32 v34, v79, v78, vcc
	s_nop 0
	v_readlane_b32 s63, v34, s63
	s_lshl_b32 s63, s63, 10
	s_add_i32 s63, s63, s62
	s_nop 2
	buffer_load_dwordx4 v[34:37], v0, s[92:95], s63 offen
	v_mov_b32_e32 v96, v1
	v_mov_b32_e32 v97, v1
	s_waitcnt vmcnt(6)
	v_dot8c_i32_i4_e32 v96, v50, v74
	v_dot8c_i32_i4_e32 v97, v50, v70
	v_dot8c_i32_i4_e32 v96, v51, v75
	v_dot8c_i32_i4_e32 v97, v51, v71
	v_dot8c_i32_i4_e32 v96, v52, v76
	v_dot8c_i32_i4_e32 v97, v52, v72
	s_add_i32 s63, s57, -1
	v_dot8c_i32_i4_e32 v96, v53, v77
	v_dot8c_i32_i4_e32 v97, v53, v73
	s_bitcmp0_b32 s63, 6
	s_cselect_b64 vcc, -1, 0
	s_nop 0
	v_lshl_add_u32 v50, v96, 4, v97
	v_cvt_f32_i32_e32 v96, v50
	v_cndmask_b32_e32 v50, v79, v78, vcc
	s_nop 0
	v_readlane_b32 s63, v50, s63
	s_lshl_b32 s63, s63, 10
	s_add_i32 s63, s63, s62
	s_nop 2
	buffer_load_dwordx4 v[50:53], v0, s[92:95], s63 offen
	v_mov_b32_e32 v97, v1
	v_mov_b32_e32 v98, v1
	s_waitcnt vmcnt(6)
	v_dot8c_i32_i4_e32 v97, v62, v74
	v_dot8c_i32_i4_e32 v98, v62, v70
	v_dot8c_i32_i4_e32 v97, v63, v75
	v_dot8c_i32_i4_e32 v98, v63, v71
	v_dot8c_i32_i4_e32 v97, v64, v76
	v_dot8c_i32_i4_e32 v98, v64, v72
	v_dot8c_i32_i4_e32 v97, v65, v77
	v_dot8c_i32_i4_e32 v98, v65, v73
	s_bitcmp0_b32 s57, 6
	s_cselect_b64 vcc, -1, 0
	s_nop 0
	v_lshl_add_u32 v62, v97, 4, v98
	v_cvt_f32_i32_e32 v97, v62
	v_cndmask_b32_e32 v62, v79, v78, vcc
	s_nop 0
	v_readlane_b32 s63, v62, s57
	s_lshl_b32 s63, s63, 10
	s_add_i32 s63, s63, s62
	s_nop 2
	buffer_load_dwordx4 v[62:65], v0, s[92:95], s63 offen
	v_cndmask_b32_e64 v98, v90, v69, s[0:1]
	v_cndmask_b32_e64 v69, v69, v90, s[0:1]
	v_cndmask_b32_e64 v90, v91, v83, s[0:1]
	v_cndmask_b32_e64 v83, v83, v91, s[0:1]
	v_cndmask_b32_e64 v91, v92, v84, s[0:1]
	v_cndmask_b32_e64 v84, v84, v92, s[0:1]
	v_cndmask_b32_e64 v92, v93, v85, s[0:1]
	v_cndmask_b32_e64 v85, v85, v93, s[0:1]
	v_cndmask_b32_e64 v93, v94, v86, s[0:1]
	v_cndmask_b32_e64 v86, v86, v94, s[0:1]
	v_cndmask_b32_e64 v94, v95, v87, s[0:1]
	v_cndmask_b32_e64 v87, v87, v95, s[0:1]
	v_cndmask_b32_e64 v95, v96, v88, s[0:1]
	v_cndmask_b32_e64 v88, v88, v96, s[0:1]
	v_cndmask_b32_e64 v96, v97, v89, s[0:1]
	v_cndmask_b32_e64 v89, v89, v97, s[0:1]
	ds_bpermute_b32 v69, v190, v69
	ds_bpermute_b32 v83, v190, v83
	ds_bpermute_b32 v84, v190, v84
	ds_bpermute_b32 v85, v190, v85
	ds_bpermute_b32 v86, v190, v86
	ds_bpermute_b32 v87, v190, v87
	ds_bpermute_b32 v88, v190, v88
	ds_bpermute_b32 v89, v190, v89
	s_waitcnt lgkmcnt(7)
; __device__ __forceinline__ int shl_i(int v, int from_lane) { return __builtin_amdgcn_ds_bpermute(from_lane << 2, v); }
;     ...
;         GATHER_U_SECTION(0, g0, w0)
;         GATHER_U_SECTION(1, g1, w1)
;         const float wm = wave_max(fmaxf(fabsf(w0), fabsf(w1)));
;         const float wsq = (wm > 0.f) ? 127.0f / wm : 0.f;
;         const int q0 = (int)rintf(w0 * wsq), q1 = (int)rintf(w1 * wsq);
;         const int c8 = 8 * (int)wave_sum((float)(q0 + q1));
;         const int pk0 = (q0 & 0xFF) | ((shl_i(q0, lane + 1) & 0xFF) << 8) | ((shl_i(q0, lane + 2) & 0xFF) << 16) | (shl_i(q0, lane + 3) << 24);
;         const int pk1 = (q1 & 0xFF) | ((shl_i(q1, lane + 1) & 0xFF) << 8) | ((shl_i(q1, lane + 2) & 0xFF) << 16) | (shl_i(q1, lane + 3) << 24);
;         int acci[32];
; #pragma unroll
;         for (int i = 0; i < 32; ++i) acci[i] = 0;
	v_add_f32_e32 v69, v98, v69
	s_waitcnt lgkmcnt(6)
	v_add_f32_e32 v83, v90, v83
	s_waitcnt lgkmcnt(5)
	v_add_f32_e32 v84, v91, v84
	s_waitcnt lgkmcnt(4)
	v_add_f32_e32 v85, v92, v85
	s_waitcnt lgkmcnt(3)
	v_add_f32_e32 v86, v93, v86
	s_waitcnt lgkmcnt(2)
	v_add_f32_e32 v87, v94, v87
	s_waitcnt lgkmcnt(1)
	v_add_f32_e32 v88, v95, v88
	s_waitcnt lgkmcnt(0)
	v_add_f32_e32 v89, v96, v89
	v_cndmask_b32_e64 v90, v86, v69, s[2:3]
	v_cndmask_b32_e64 v69, v69, v86, s[2:3]
	v_cndmask_b32_e64 v86, v87, v83, s[2:3]
	v_cndmask_b32_e64 v83, v83, v87, s[2:3]
	v_cndmask_b32_e64 v87, v88, v84, s[2:3]
	v_cndmask_b32_e64 v84, v84, v88, s[2:3]
	v_cndmask_b32_e64 v88, v89, v85, s[2:3]
	v_cndmask_b32_e64 v85, v85, v89, s[2:3]
	ds_bpermute_b32 v69, v189, v69
	ds_bpermute_b32 v83, v189, v83
	ds_bpermute_b32 v84, v189, v84
	ds_bpermute_b32 v85, v189, v85
	s_add_i32 s57, s57, 16
	s_waitcnt lgkmcnt(3)
	v_add_f32_e32 v69, v90, v69
	s_waitcnt lgkmcnt(2)
	v_add_f32_e32 v83, v86, v83
	s_waitcnt lgkmcnt(1)
	v_add_f32_e32 v84, v87, v84
	s_waitcnt lgkmcnt(0)
	v_add_f32_e32 v85, v88, v85
	v_cndmask_b32_e64 v86, v84, v69, s[4:5]
	v_cndmask_b32_e64 v69, v69, v84, s[4:5]
	v_cndmask_b32_e64 v84, v85, v83, s[4:5]
	v_cndmask_b32_e64 v83, v83, v85, s[4:5]
	ds_bpermute_b32 v69, v188, v69
	ds_bpermute_b32 v83, v188, v83
	s_waitcnt lgkmcnt(1)
	v_add_f32_e32 v69, v86, v69
	s_waitcnt lgkmcnt(0)
	v_add_f32_e32 v83, v84, v83
	v_cndmask_b32_e64 v84, v83, v69, s[6:7]
	v_cndmask_b32_e64 v69, v69, v83, s[6:7]
	ds_bpermute_b32 v69, v163, v69
	s_waitcnt lgkmcnt(0)
	v_add_f32_e32 v69, v84, v69
	v_mov_b32_e32 v83, v69
	s_nop 1
	v_permlane16_swap_b32_e32 v69, v83
	v_add_f32_e32 v69, v69, v83
	v_mov_b32_e32 v83, v69
	s_nop 1
	v_permlane32_swap_b32_e32 v69, v83
	v_add_f32_e32 v69, v69, v83
	v_mul_f32_e32 v69, v66, v69
	v_fma_f32 v83, |v69|, s66, 1.0
	v_rcp_f32_e32 v83, v83
	v_mul_f32_e32 v84, v69, v69
	v_mul_f32_e32 v84, 0xbf38aa3b, v84
	v_exp_f32_e32 v84, v84
	v_fmamk_f32 v85, v83, 0x3f07dc22, v207
	v_fmaak_f32 v85, v83, v85, 0x3f35f0e3
	v_fmaak_f32 v85, v83, v85, 0xbe11a98e
	v_fmaak_f32 v85, v83, v85, 0x3e027906
	v_mul_f32_e32 v83, v83, v85
	v_mul_f32_e32 v83, v84, v83
	v_mul_f32_e32 v84, v69, v83
	v_fma_f32 v83, -v69, v83, v69
	v_cmp_gt_f32_e32 vcc, 0, v69
	s_nop 1
	v_cndmask_b32_e32 v69, v83, v84, vcc
	v_mul_f32_e32 v69, 0x3d4ccccd, v69
	v_mul_f32_e32 v69, v80, v69
	v_cmp_eq_u32_e32 vcc, s56, v193
	s_add_i32 s56, s56, 1
	s_cmpk_eq_i32 s57, 0x9f
	v_cndmask_b32_e32 v82, v82, v69, vcc
	s_cbranch_scc0 .LBB0_1421
	v_max_f32_e64 v66, |v82|, |v82|
	v_max_f32_e64 v69, |v81|, |v81|
	v_max_f32_e32 v66, v69, v66
	v_mov_b32_e32 v69, 0
	s_mov_b32 s57, 0x42fe0000
	v_mbcnt_lo_u32_b32 v69, -1, v69
	v_mbcnt_hi_u32_b32 v69, -1, v69
	v_lshlrev_b32_e32 v71, 2, v69
	v_xor_b32_e32 v69, 0x80, v71
	ds_bpermute_b32 v69, v69, v66
	v_xor_b32_e32 v70, 64, v71
	v_xor_b32_e32 v72, 8, v71
	v_mov_b32_e32 v83, 0
	s_waitcnt lgkmcnt(0)
	v_max_f32_e32 v69, v69, v69
	v_max_f32_e32 v66, v66, v69
	ds_bpermute_b32 v69, v70, v66
	v_xor_b32_e32 v70, 32, v71
	s_movk_i32 s56, 0x9f
	v_mov_b32_e32 v74, 0
	v_mov_b32_e32 v75, 0
	s_waitcnt lgkmcnt(0)
	v_max_f32_e32 v69, v69, v69
	v_max_f32_e32 v66, v66, v69
	ds_bpermute_b32 v69, v70, v66
	v_xor_b32_e32 v70, 16, v71
	v_xor_b32_e32 v71, 4, v71
	v_mov_b32_e32 v76, 0
	v_mov_b32_e32 v80, 0
	s_waitcnt lgkmcnt(0)
	v_max_f32_e32 v69, v69, v69
	v_max_f32_e32 v69, v66, v69
	ds_bpermute_b32 v70, v70, v69
	v_mov_b32_e32 v66, 0
	v_mov_b32_e32 v94, 0
	v_mov_b32_e32 v95, 0
	v_mov_b32_e32 v96, 0
	s_waitcnt lgkmcnt(0)
	v_max_f32_e32 v70, v70, v70
	v_max_f32_e32 v73, v69, v70
	ds_bpermute_b32 v72, v72, v73
	v_mov_b32_e32 v69, 0
	v_mov_b32_e32 v70, 0
	v_mov_b32_e32 v97, 0
	v_mov_b32_e32 v98, 0
	s_waitcnt lgkmcnt(0)
	v_max_f32_e32 v72, v72, v72
	v_max_f32_e32 v77, v73, v72
	ds_bpermute_b32 v71, v71, v77
	v_mov_b32_e32 v72, 0
	v_mov_b32_e32 v73, 0
	v_mov_b32_e32 v99, 0
	v_mov_b32_e32 v100, 0
	s_waitcnt lgkmcnt(0)
	v_max_f32_e32 v71, v71, v71
	v_max_f32_e32 v71, v77, v71
	v_div_scale_f32 v77, s[62:63], v71, v71, s57
	v_rcp_f32_e32 v84, v77
	v_div_scale_f32 v85, vcc, s57, v71, s57
	v_mov_b32_e32 v101, 0
	v_fma_f32 v86, -v77, v84, 1.0
	v_fmac_f32_e32 v84, v86, v84
	v_mul_f32_e32 v86, v85, v84
	v_fma_f32 v87, -v77, v86, v85
	v_fmac_f32_e32 v86, v87, v84
	v_fma_f32 v77, -v77, v86, v85
	v_div_fmas_f32 v77, v77, v84, v86
	v_div_fixup_f32 v77, v77, v71, s57
	v_cmp_lt_f32_e32 vcc, 0, v71
	s_mov_b32 s57, 0xc0c0500
	v_mov_b32_e32 v85, 0
	v_cndmask_b32_e32 v77, 0, v77, vcc
	v_mul_f32_e32 v81, v81, v77
	v_mul_f32_e32 v77, v82, v77
	v_rndne_f32_e32 v81, v81
	v_rndne_f32_e32 v77, v77
	v_cvt_i32_f32_e32 v82, v81
	v_cvt_i32_f32_e32 v107, v77
	v_mbcnt_lo_u32_b32 v81, -1, v83
	v_mbcnt_hi_u32_b32 v81, -1, v81
	v_lshlrev_b32_e32 v84, 2, v81
	v_add_u32_e32 v83, v82, v107
	v_cvt_f32_i32_e32 v83, v83
	v_xor_b32_e32 v81, 0x80, v84
	v_xor_b32_e32 v88, 64, v84
	v_xor_b32_e32 v89, 16, v84
	ds_bpermute_b32 v87, v81, v83
	v_xor_b32_e32 v90, 8, v84
	ds_bpermute_b32 v91, v195, v82
	ds_bpermute_b32 v92, v196, v82
	ds_bpermute_b32 v108, v194, v107
	s_waitcnt lgkmcnt(3)
	v_add_f32_e32 v83, v87, v83
	ds_bpermute_b32 v87, v88, v83
	v_xor_b32_e32 v88, 32, v84
	v_xor_b32_e32 v84, 4, v84
	ds_bpermute_b32 v109, v195, v107
	ds_bpermute_b32 v110, v196, v107
	s_waitcnt lgkmcnt(2)
	v_add_f32_e32 v83, v83, v87
	ds_bpermute_b32 v87, v88, v83
	ds_bpermute_b32 v88, v194, v82
	v_mov_b32_e32 v77, 0
	v_mov_b32_e32 v81, 0
	v_mov_b32_e32 v86, 0
	s_waitcnt lgkmcnt(1)
	v_add_f32_e32 v83, v83, v87
	ds_bpermute_b32 v87, v89, v83
	s_waitcnt lgkmcnt(1)
	v_lshlrev_b32_e32 v88, 8, v88
	v_lshlrev_b32_e32 v89, 16, v91
	v_perm_b32 v82, v88, v82, s57
	v_and_b32_e32 v88, 0xff0000, v89
	s_waitcnt lgkmcnt(0)
	v_add_f32_e32 v83, v83, v87
	ds_bpermute_b32 v87, v90, v83
	v_lshlrev_b32_e32 v90, 24, v92
	v_or3_b32 v111, v82, v88, v90
	v_mov_b32_e32 v82, 0
	v_mov_b32_e32 v88, 0
	s_waitcnt lgkmcnt(0)
	v_add_f32_e32 v103, v83, v87
	ds_bpermute_b32 v104, v84, v103
	v_mov_b32_e32 v84, 0
	v_mov_b32_e32 v87, 0
	v_mov_b32_e32 v89, 0
	v_mov_b32_e32 v90, 0
	v_mov_b32_e32 v91, 0
	v_mov_b32_e32 v92, 0
	v_mov_b32_e32 v93, 0
	v_mov_b32_e32 v102, 0
	v_mov_b32_e32 v83, 0
	s_barrier
.LBB0_1423:
	s_add_i32 s57, s56, 0xffffff61
	s_waitcnt vmcnt(5)
	v_perm_b32 v112, v14, v6, s67
	v_perm_b32 v6, v14, v6, s68
	s_waitcnt vmcnt(3)
	v_perm_b32 v14, v46, v30, s67
	v_readlane_b32 s57, v111, s57
	v_perm_b32 v30, v46, v30, s68
	v_perm_b32 v46, v14, v112, s69
	v_perm_b32 v14, v14, v112, s33
	v_perm_b32 v112, v30, v6, s69
	v_perm_b32 v6, v30, v6, s33
	v_dot4c_i32_i8_e32 v74, s57, v14
	v_and_b32_e32 v14, 0xf0f0f0f0, v14
	v_dot4c_i32_i8_e32 v70, s57, v14
	v_and_b32_e32 v14, 0xf0f0f0f0, v112
	v_dot4c_i32_i8_e32 v76, s57, v6
	v_and_b32_e32 v6, 0xf0f0f0f0, v6
	v_and_b32_e32 v30, 0xf0f0f0f0, v46
	v_dot4c_i32_i8_e32 v72, s57, v14
	v_dot4c_i32_i8_e32 v73, s57, v6
	v_perm_b32 v6, v15, v7, s67
	v_perm_b32 v14, v47, v31, s67
	v_dot4c_i32_i8_e32 v69, s57, v30
	v_perm_b32 v7, v15, v7, s68
	v_perm_b32 v15, v47, v31, s68
	v_perm_b32 v30, v14, v6, s69
	v_perm_b32 v6, v14, v6, s33
	v_perm_b32 v14, v15, v7, s69
	v_dot4c_i32_i8_e32 v85, s57, v6
	v_and_b32_e32 v6, 0xf0f0f0f0, v6
	v_perm_b32 v7, v15, v7, s33
	v_dot4c_i32_i8_e32 v81, s57, v6
	v_and_b32_e32 v6, 0xf0f0f0f0, v14
	v_dot4c_i32_i8_e32 v82, s57, v6
	v_and_b32_e32 v6, 0xf0f0f0f0, v7
	v_and_b32_e32 v15, 0xf0f0f0f0, v30
	v_dot4c_i32_i8_e32 v94, s57, v7
	v_dot4c_i32_i8_e32 v84, s57, v6
	v_perm_b32 v6, v16, v8, s67
	v_perm_b32 v7, v16, v8, s68
	v_perm_b32 v8, v48, v32, s67
	v_dot4c_i32_i8_e32 v77, s57, v15
	v_dot4c_i32_i8_e32 v86, s57, v14
	v_perm_b32 v14, v48, v32, s68
	v_perm_b32 v15, v8, v6, s69
	v_perm_b32 v6, v8, v6, s33
	v_perm_b32 v8, v14, v7, s69
	v_dot4c_i32_i8_e32 v96, s57, v6
	v_and_b32_e32 v6, 0xf0f0f0f0, v6
	v_perm_b32 v7, v14, v7, s33
	v_dot4c_i32_i8_e32 v88, s57, v6
	v_and_b32_e32 v6, 0xf0f0f0f0, v8
	v_dot4c_i32_i8_e32 v89, s57, v6
	v_and_b32_e32 v6, 0xf0f0f0f0, v7
	v_and_b32_e32 v14, 0xf0f0f0f0, v15
	v_dot4c_i32_i8_e32 v97, s57, v8
	v_dot4c_i32_i8_e32 v90, s57, v6
	v_perm_b32 v6, v17, v9, s67
	v_perm_b32 v8, v49, v33, s67
	v_dot4c_i32_i8_e32 v87, s57, v14
	v_dot4c_i32_i8_e32 v98, s57, v7
	v_perm_b32 v7, v17, v9, s68
	v_perm_b32 v9, v49, v33, s68
	v_perm_b32 v14, v8, v6, s69
	v_perm_b32 v6, v8, v6, s33
	v_perm_b32 v8, v9, v7, s69
	v_dot4c_i32_i8_e32 v100, s57, v6
	v_and_b32_e32 v6, 0xf0f0f0f0, v6
	v_perm_b32 v7, v9, v7, s33
	v_dot4c_i32_i8_e32 v92, s57, v6
	v_and_b32_e32 v6, 0xf0f0f0f0, v8
	v_and_b32_e32 v9, 0xf0f0f0f0, v14
	v_dot4c_i32_i8_e32 v93, s57, v6
	v_and_b32_e32 v6, 0xf0f0f0f0, v7
	v_dot4c_i32_i8_e32 v66, s57, v46
	v_dot4c_i32_i8_e32 v75, s57, v112
	v_dot4c_i32_i8_e32 v80, s57, v30
	v_dot4c_i32_i8_e32 v95, s57, v15
	v_dot4c_i32_i8_e32 v99, s57, v14
	v_dot4c_i32_i8_e32 v91, s57, v9
	v_dot4c_i32_i8_e32 v101, s57, v8
	v_dot4c_i32_i8_e32 v102, s57, v7
	v_dot4c_i32_i8_e32 v83, s57, v6
	s_add_i32 s57, s56, -15
	s_bitcmp0_b32 s57, 6
	s_cselect_b64 vcc, -1, 0
	v_cndmask_b32_e32 v6, v79, v78, vcc
	s_nop 0
	v_readlane_b32 s57, v6, s57
	s_lshl_b32 s57, s57, 10
	s_add_i32 s57, s57, 0x1000000
	s_nop 2
	buffer_load_dwordx4 v[6:9], v0, s[92:95], s57 offen
	s_add_i32 s57, s56, -14
	s_bitcmp0_b32 s57, 6
	s_cselect_b64 vcc, -1, 0
	v_cndmask_b32_e32 v14, v79, v78, vcc
	s_nop 0
	v_readlane_b32 s57, v14, s57
	s_lshl_b32 s57, s57, 10
	s_add_i32 s57, s57, 0x1000000
	s_nop 2
	buffer_load_dwordx4 v[14:17], v0, s[92:95], s57 offen
	s_add_i32 s57, s56, -13
	s_bitcmp0_b32 s57, 6
	s_cselect_b64 vcc, -1, 0
	v_cndmask_b32_e32 v30, v79, v78, vcc
	s_nop 0
	v_readlane_b32 s57, v30, s57
	s_lshl_b32 s57, s57, 10
	s_add_i32 s57, s57, 0x1000000
	s_nop 2
	buffer_load_dwordx4 v[30:33], v0, s[92:95], s57 offen
	s_add_i32 s57, s56, -12
	s_bitcmp0_b32 s57, 6
	s_cselect_b64 vcc, -1, 0
	v_cndmask_b32_e32 v46, v79, v78, vcc
	s_nop 0
	v_readlane_b32 s57, v46, s57
	s_lshl_b32 s57, s57, 10
	s_add_i32 s57, s57, 0x1000000
	s_nop 2
	buffer_load_dwordx4 v[46:49], v0, s[92:95], s57 offen
	s_add_i32 s57, s56, 0xffffff65
	s_waitcnt vmcnt(5)
	v_perm_b32 v112, v22, v2, s67
	v_perm_b32 v2, v22, v2, s68
	s_waitcnt vmcnt(3)
	v_perm_b32 v22, v54, v38, s67
	v_readlane_b32 s57, v111, s57
	v_perm_b32 v38, v54, v38, s68
	v_perm_b32 v54, v22, v112, s69
	v_perm_b32 v22, v22, v112, s33
	v_perm_b32 v112, v38, v2, s69
	v_perm_b32 v2, v38, v2, s33
	v_dot4c_i32_i8_e32 v74, s57, v22
	v_and_b32_e32 v22, 0xf0f0f0f0, v22
	v_dot4c_i32_i8_e32 v70, s57, v22
	v_and_b32_e32 v22, 0xf0f0f0f0, v112
	v_dot4c_i32_i8_e32 v76, s57, v2
	v_and_b32_e32 v2, 0xf0f0f0f0, v2
	v_and_b32_e32 v38, 0xf0f0f0f0, v54
	v_dot4c_i32_i8_e32 v72, s57, v22
	v_dot4c_i32_i8_e32 v73, s57, v2
	v_perm_b32 v2, v23, v3, s67
	v_perm_b32 v22, v55, v39, s67
	v_dot4c_i32_i8_e32 v69, s57, v38
	v_perm_b32 v3, v23, v3, s68
	v_perm_b32 v23, v55, v39, s68
	v_perm_b32 v38, v22, v2, s69
	v_perm_b32 v2, v22, v2, s33
	v_perm_b32 v22, v23, v3, s69
	v_dot4c_i32_i8_e32 v85, s57, v2
	v_and_b32_e32 v2, 0xf0f0f0f0, v2
	v_perm_b32 v3, v23, v3, s33
	v_dot4c_i32_i8_e32 v81, s57, v2
	v_and_b32_e32 v2, 0xf0f0f0f0, v22
	v_dot4c_i32_i8_e32 v82, s57, v2
	v_and_b32_e32 v2, 0xf0f0f0f0, v3
	v_and_b32_e32 v23, 0xf0f0f0f0, v38
	v_dot4c_i32_i8_e32 v94, s57, v3
	v_dot4c_i32_i8_e32 v84, s57, v2
	v_perm_b32 v2, v24, v4, s67
	v_perm_b32 v3, v24, v4, s68
	v_perm_b32 v4, v56, v40, s67
	v_dot4c_i32_i8_e32 v77, s57, v23
	v_dot4c_i32_i8_e32 v86, s57, v22
	v_perm_b32 v22, v56, v40, s68
	v_perm_b32 v23, v4, v2, s69
	v_perm_b32 v2, v4, v2, s33
	v_perm_b32 v4, v22, v3, s69
	v_dot4c_i32_i8_e32 v96, s57, v2
	v_and_b32_e32 v2, 0xf0f0f0f0, v2
	v_perm_b32 v3, v22, v3, s33
	v_dot4c_i32_i8_e32 v88, s57, v2
	v_and_b32_e32 v2, 0xf0f0f0f0, v4
	v_dot4c_i32_i8_e32 v89, s57, v2
	v_and_b32_e32 v2, 0xf0f0f0f0, v3
	v_and_b32_e32 v22, 0xf0f0f0f0, v23
	v_dot4c_i32_i8_e32 v97, s57, v4
	v_dot4c_i32_i8_e32 v90, s57, v2
	v_perm_b32 v2, v25, v5, s67
	v_perm_b32 v4, v57, v41, s67
	v_dot4c_i32_i8_e32 v87, s57, v22
	v_dot4c_i32_i8_e32 v98, s57, v3
	v_perm_b32 v3, v25, v5, s68
	v_perm_b32 v5, v57, v41, s68
	v_perm_b32 v22, v4, v2, s69
	v_perm_b32 v2, v4, v2, s33
	v_perm_b32 v4, v5, v3, s69
	v_dot4c_i32_i8_e32 v100, s57, v2
	v_and_b32_e32 v2, 0xf0f0f0f0, v2
	v_perm_b32 v3, v5, v3, s33
	v_dot4c_i32_i8_e32 v92, s57, v2
	v_and_b32_e32 v2, 0xf0f0f0f0, v4
	v_and_b32_e32 v5, 0xf0f0f0f0, v22
	v_dot4c_i32_i8_e32 v93, s57, v2
	v_and_b32_e32 v2, 0xf0f0f0f0, v3
	v_dot4c_i32_i8_e32 v66, s57, v54
	v_dot4c_i32_i8_e32 v75, s57, v112
	v_dot4c_i32_i8_e32 v80, s57, v38
	v_dot4c_i32_i8_e32 v95, s57, v23
	v_dot4c_i32_i8_e32 v99, s57, v22
	v_dot4c_i32_i8_e32 v91, s57, v5
	v_dot4c_i32_i8_e32 v101, s57, v4
	v_dot4c_i32_i8_e32 v102, s57, v3
	v_dot4c_i32_i8_e32 v83, s57, v2
	s_add_i32 s57, s56, -11
	s_bitcmp0_b32 s57, 6
	s_cselect_b64 vcc, -1, 0
	v_cndmask_b32_e32 v2, v79, v78, vcc
	s_nop 0
	v_readlane_b32 s57, v2, s57
	s_lshl_b32 s57, s57, 10
	s_add_i32 s57, s57, 0x1000000
	s_nop 2
	buffer_load_dwordx4 v[2:5], v0, s[92:95], s57 offen
	s_add_i32 s57, s56, -10
	s_bitcmp0_b32 s57, 6
	s_cselect_b64 vcc, -1, 0
	v_cndmask_b32_e32 v22, v79, v78, vcc
	s_nop 0
	v_readlane_b32 s57, v22, s57
	s_lshl_b32 s57, s57, 10
	s_add_i32 s57, s57, 0x1000000
	s_nop 2
	buffer_load_dwordx4 v[22:25], v0, s[92:95], s57 offen
	s_add_i32 s57, s56, -9
	s_bitcmp0_b32 s57, 6
	s_cselect_b64 vcc, -1, 0
	v_cndmask_b32_e32 v38, v79, v78, vcc
	s_nop 0
	v_readlane_b32 s57, v38, s57
	s_lshl_b32 s57, s57, 10
	s_add_i32 s57, s57, 0x1000000
	s_nop 2
	buffer_load_dwordx4 v[38:41], v0, s[92:95], s57 offen
	s_add_i32 s57, s56, -8
	s_bitcmp0_b32 s57, 6
	s_cselect_b64 vcc, -1, 0
	v_cndmask_b32_e32 v54, v79, v78, vcc
	s_nop 0
	v_readlane_b32 s57, v54, s57
	s_lshl_b32 s57, s57, 10
	s_add_i32 s57, s57, 0x1000000
	s_nop 2
	buffer_load_dwordx4 v[54:57], v0, s[92:95], s57 offen
	s_add_i32 s57, s56, 0xffffff69
	s_waitcnt vmcnt(5)
	v_perm_b32 v112, v26, v10, s67
	v_perm_b32 v10, v26, v10, s68
	s_waitcnt vmcnt(3)
	v_perm_b32 v26, v58, v42, s67
	v_readlane_b32 s57, v111, s57
	v_perm_b32 v42, v58, v42, s68
	v_perm_b32 v58, v26, v112, s69
	v_perm_b32 v26, v26, v112, s33
	v_perm_b32 v112, v42, v10, s69
	v_perm_b32 v10, v42, v10, s33
	v_dot4c_i32_i8_e32 v74, s57, v26
	v_and_b32_e32 v26, 0xf0f0f0f0, v26
	v_dot4c_i32_i8_e32 v70, s57, v26
	v_and_b32_e32 v26, 0xf0f0f0f0, v112
	v_dot4c_i32_i8_e32 v76, s57, v10
	v_and_b32_e32 v10, 0xf0f0f0f0, v10
	v_and_b32_e32 v42, 0xf0f0f0f0, v58
	v_dot4c_i32_i8_e32 v72, s57, v26
	v_dot4c_i32_i8_e32 v73, s57, v10
	v_perm_b32 v10, v27, v11, s67
	v_perm_b32 v26, v59, v43, s67
	v_dot4c_i32_i8_e32 v69, s57, v42
	v_perm_b32 v11, v27, v11, s68
	v_perm_b32 v27, v59, v43, s68
	v_perm_b32 v42, v26, v10, s69
	v_perm_b32 v10, v26, v10, s33
	v_perm_b32 v26, v27, v11, s69
	v_dot4c_i32_i8_e32 v85, s57, v10
	v_and_b32_e32 v10, 0xf0f0f0f0, v10
	v_perm_b32 v11, v27, v11, s33
	v_dot4c_i32_i8_e32 v81, s57, v10
	v_and_b32_e32 v10, 0xf0f0f0f0, v26
	v_dot4c_i32_i8_e32 v82, s57, v10
	v_and_b32_e32 v10, 0xf0f0f0f0, v11
	v_and_b32_e32 v27, 0xf0f0f0f0, v42
	v_dot4c_i32_i8_e32 v94, s57, v11
	v_dot4c_i32_i8_e32 v84, s57, v10
	v_perm_b32 v10, v28, v12, s67
	v_perm_b32 v11, v28, v12, s68
	v_perm_b32 v12, v60, v44, s67
	v_dot4c_i32_i8_e32 v77, s57, v27
	v_dot4c_i32_i8_e32 v86, s57, v26
	v_perm_b32 v26, v60, v44, s68
	v_perm_b32 v27, v12, v10, s69
	v_perm_b32 v10, v12, v10, s33
	v_perm_b32 v12, v26, v11, s69
	v_dot4c_i32_i8_e32 v96, s57, v10
	v_and_b32_e32 v10, 0xf0f0f0f0, v10
	v_perm_b32 v11, v26, v11, s33
	v_dot4c_i32_i8_e32 v88, s57, v10
	v_and_b32_e32 v10, 0xf0f0f0f0, v12
	v_dot4c_i32_i8_e32 v89, s57, v10
	v_and_b32_e32 v10, 0xf0f0f0f0, v11
	v_and_b32_e32 v26, 0xf0f0f0f0, v27
	v_dot4c_i32_i8_e32 v97, s57, v12
	v_dot4c_i32_i8_e32 v90, s57, v10
	v_perm_b32 v10, v29, v13, s67
	v_perm_b32 v12, v61, v45, s67
	v_dot4c_i32_i8_e32 v87, s57, v26
	v_dot4c_i32_i8_e32 v98, s57, v11
	v_perm_b32 v11, v29, v13, s68
	v_perm_b32 v13, v61, v45, s68
	v_perm_b32 v26, v12, v10, s69
	v_perm_b32 v10, v12, v10, s33
	v_perm_b32 v12, v13, v11, s69
	v_dot4c_i32_i8_e32 v100, s57, v10
	v_and_b32_e32 v10, 0xf0f0f0f0, v10
	v_perm_b32 v11, v13, v11, s33
	v_dot4c_i32_i8_e32 v92, s57, v10
	v_and_b32_e32 v10, 0xf0f0f0f0, v12
	v_and_b32_e32 v13, 0xf0f0f0f0, v26
	v_dot4c_i32_i8_e32 v93, s57, v10
	v_and_b32_e32 v10, 0xf0f0f0f0, v11
	v_dot4c_i32_i8_e32 v66, s57, v58
	v_dot4c_i32_i8_e32 v75, s57, v112
	v_dot4c_i32_i8_e32 v80, s57, v42
	v_dot4c_i32_i8_e32 v95, s57, v27
	v_dot4c_i32_i8_e32 v99, s57, v26
	v_dot4c_i32_i8_e32 v91, s57, v13
	v_dot4c_i32_i8_e32 v101, s57, v12
	v_dot4c_i32_i8_e32 v102, s57, v11
	v_dot4c_i32_i8_e32 v83, s57, v10
	s_add_i32 s57, s56, -7
	s_bitcmp0_b32 s57, 6
	s_cselect_b64 vcc, -1, 0
	v_cndmask_b32_e32 v10, v79, v78, vcc
	s_nop 0
	v_readlane_b32 s57, v10, s57
	s_lshl_b32 s57, s57, 10
	s_add_i32 s57, s57, 0x1000000
	s_nop 2
	buffer_load_dwordx4 v[10:13], v0, s[92:95], s57 offen
	s_add_i32 s57, s56, -6
	s_bitcmp0_b32 s57, 6
	s_cselect_b64 vcc, -1, 0
	v_cndmask_b32_e32 v26, v79, v78, vcc
	s_nop 0
	v_readlane_b32 s57, v26, s57
	s_lshl_b32 s57, s57, 10
	s_add_i32 s57, s57, 0x1000000
	s_nop 2
	buffer_load_dwordx4 v[26:29], v0, s[92:95], s57 offen
	s_add_i32 s57, s56, -5
	s_bitcmp0_b32 s57, 6
	s_cselect_b64 vcc, -1, 0
	v_cndmask_b32_e32 v42, v79, v78, vcc
	s_nop 0
	v_readlane_b32 s57, v42, s57
	s_lshl_b32 s57, s57, 10
	s_add_i32 s57, s57, 0x1000000
	s_nop 2
	buffer_load_dwordx4 v[42:45], v0, s[92:95], s57 offen
	s_add_i32 s57, s56, -4
	s_bitcmp0_b32 s57, 6
	s_cselect_b64 vcc, -1, 0
	v_cndmask_b32_e32 v58, v79, v78, vcc
	s_nop 0
	v_readlane_b32 s57, v58, s57
	s_lshl_b32 s57, s57, 10
	s_add_i32 s57, s57, 0x1000000
	s_nop 2
	buffer_load_dwordx4 v[58:61], v0, s[92:95], s57 offen
	s_add_i32 s57, s56, 0xffffff6d
	s_waitcnt vmcnt(5)
; __device__ __forceinline__ int shl_i(int v, int from_lane) { return __builtin_amdgcn_ds_bpermute(from_lane << 2, v); }
;     ...
;         const int pk1 = (q1 & 0xFF) | ((shl_i(q1, lane + 1) & 0xFF) << 8) | ((shl_i(q1, lane + 2) & 0xFF) << 16) | (shl_i(q1, lane + 3) << 24);
;     ...
;         GATHER_V_SECTION(2, pk0)
;         GATHER_V_SECTION(3, pk1)
	v_perm_b32 v112, v34, v18, s67
	v_perm_b32 v18, v34, v18, s68
	s_waitcnt vmcnt(3)
	v_perm_b32 v34, v62, v50, s67
	v_readlane_b32 s57, v111, s57
	v_perm_b32 v50, v62, v50, s68
	v_perm_b32 v62, v34, v112, s69
	v_perm_b32 v34, v34, v112, s33
	v_perm_b32 v112, v50, v18, s69
	v_perm_b32 v18, v50, v18, s33
	v_dot4c_i32_i8_e32 v74, s57, v34
	v_and_b32_e32 v34, 0xf0f0f0f0, v34
	v_dot4c_i32_i8_e32 v70, s57, v34
	v_and_b32_e32 v34, 0xf0f0f0f0, v112
	v_dot4c_i32_i8_e32 v76, s57, v18
	v_and_b32_e32 v18, 0xf0f0f0f0, v18
	v_and_b32_e32 v50, 0xf0f0f0f0, v62
	v_dot4c_i32_i8_e32 v72, s57, v34
	v_dot4c_i32_i8_e32 v73, s57, v18
	v_perm_b32 v18, v35, v19, s67
	v_perm_b32 v34, v63, v51, s67
	v_dot4c_i32_i8_e32 v69, s57, v50
	v_perm_b32 v19, v35, v19, s68
	v_perm_b32 v35, v63, v51, s68
	v_perm_b32 v50, v34, v18, s69
	v_perm_b32 v18, v34, v18, s33
	v_perm_b32 v34, v35, v19, s69
	v_dot4c_i32_i8_e32 v85, s57, v18
	v_and_b32_e32 v18, 0xf0f0f0f0, v18
	v_perm_b32 v19, v35, v19, s33
	v_dot4c_i32_i8_e32 v81, s57, v18
	v_and_b32_e32 v18, 0xf0f0f0f0, v34
	v_dot4c_i32_i8_e32 v82, s57, v18
	v_and_b32_e32 v18, 0xf0f0f0f0, v19
	v_and_b32_e32 v35, 0xf0f0f0f0, v50
	v_dot4c_i32_i8_e32 v94, s57, v19
	v_dot4c_i32_i8_e32 v84, s57, v18
	v_perm_b32 v18, v36, v20, s67
	v_perm_b32 v19, v36, v20, s68
	v_perm_b32 v20, v64, v52, s67
	v_dot4c_i32_i8_e32 v77, s57, v35
	v_dot4c_i32_i8_e32 v86, s57, v34
	v_perm_b32 v34, v64, v52, s68
	v_perm_b32 v35, v20, v18, s69
	v_perm_b32 v18, v20, v18, s33
	v_perm_b32 v20, v34, v19, s69
	v_dot4c_i32_i8_e32 v96, s57, v18
	v_and_b32_e32 v18, 0xf0f0f0f0, v18
	v_perm_b32 v19, v34, v19, s33
	v_dot4c_i32_i8_e32 v88, s57, v18
	v_and_b32_e32 v18, 0xf0f0f0f0, v20
	v_dot4c_i32_i8_e32 v89, s57, v18
	v_and_b32_e32 v18, 0xf0f0f0f0, v19
	v_and_b32_e32 v34, 0xf0f0f0f0, v35
	v_dot4c_i32_i8_e32 v97, s57, v20
	v_dot4c_i32_i8_e32 v90, s57, v18
	v_perm_b32 v18, v37, v21, s67
	v_perm_b32 v20, v65, v53, s67
	v_dot4c_i32_i8_e32 v87, s57, v34
	v_dot4c_i32_i8_e32 v98, s57, v19
	v_perm_b32 v19, v37, v21, s68
	v_perm_b32 v21, v65, v53, s68
	v_perm_b32 v34, v20, v18, s69
	v_perm_b32 v18, v20, v18, s33
	v_perm_b32 v20, v21, v19, s69
	v_dot4c_i32_i8_e32 v100, s57, v18
	v_and_b32_e32 v18, 0xf0f0f0f0, v18
	v_perm_b32 v19, v21, v19, s33
	v_dot4c_i32_i8_e32 v92, s57, v18
	v_and_b32_e32 v18, 0xf0f0f0f0, v20
	v_and_b32_e32 v21, 0xf0f0f0f0, v34
	v_dot4c_i32_i8_e32 v93, s57, v18
	v_and_b32_e32 v18, 0xf0f0f0f0, v19
	v_dot4c_i32_i8_e32 v66, s57, v62
	v_dot4c_i32_i8_e32 v75, s57, v112
	v_dot4c_i32_i8_e32 v80, s57, v50
	v_dot4c_i32_i8_e32 v95, s57, v35
	v_dot4c_i32_i8_e32 v99, s57, v34
	v_dot4c_i32_i8_e32 v91, s57, v21
	v_dot4c_i32_i8_e32 v101, s57, v20
	v_dot4c_i32_i8_e32 v102, s57, v19
	v_dot4c_i32_i8_e32 v83, s57, v18
	s_add_i32 s57, s56, -3
	s_bitcmp0_b32 s57, 6
	s_cselect_b64 vcc, -1, 0
	v_cndmask_b32_e32 v18, v79, v78, vcc
	s_nop 0
	v_readlane_b32 s57, v18, s57
	s_lshl_b32 s57, s57, 10
	s_add_i32 s57, s57, 0x1000000
	s_nop 2
	buffer_load_dwordx4 v[18:21], v0, s[92:95], s57 offen
	s_add_i32 s57, s56, -2
	s_bitcmp0_b32 s57, 6
	s_cselect_b64 vcc, -1, 0
	v_cndmask_b32_e32 v34, v79, v78, vcc
	s_nop 0
	v_readlane_b32 s57, v34, s57
	s_lshl_b32 s57, s57, 10
	s_add_i32 s57, s57, 0x1000000
	s_nop 2
	buffer_load_dwordx4 v[34:37], v0, s[92:95], s57 offen
	s_add_i32 s57, s56, -1
	s_bitcmp0_b32 s57, 6
	s_cselect_b64 vcc, -1, 0
	v_cndmask_b32_e32 v50, v79, v78, vcc
	s_nop 0
	v_readlane_b32 s57, v50, s57
	s_lshl_b32 s57, s57, 10
	s_add_i32 s57, s57, 0x1000000
	s_bitcmp0_b32 s56, 6
	s_cselect_b64 vcc, -1, 0
	v_cndmask_b32_e32 v62, v79, v78, vcc
	buffer_load_dwordx4 v[50:53], v0, s[92:95], s57 offen
	v_readlane_b32 s57, v62, s56
	s_lshl_b32 s57, s57, 10
	s_add_i32 s57, s57, 0x1000000
	s_nop 2
	buffer_load_dwordx4 v[62:65], v0, s[92:95], s57 offen
	s_add_i32 s56, s56, 16
	s_cmpk_lg_i32 s56, 0xdf
	s_cbranch_scc1 .LBB0_1423
	v_min_u32_e32 v111, v105, v106
	v_max_u32_e32 v105, v105, v106
	v_cndmask_b32_e64 v200, v105, v111, s[6:7]
	v_lshlrev_b32_e32 v105, 8, v108
	v_lshlrev_b32_e32 v106, 16, v109
	s_mov_b32 s56, 0xc0c0500
	v_lshlrev_b32_e32 v108, 24, v110
	v_perm_b32 v105, v105, v107, s56
	v_and_b32_e32 v106, 0xff0000, v106
	v_lshrrev_b32_e32 v199, 16, v200
	v_or3_b32 v105, v105, v106, v108
	s_mov_b32 s62, 0
	s_movk_i32 s63, 0xdf
	s_mov_b32 s90, 0x1be0000
	s_barrier
